# v56 + s_setprio 2 for k_prep G/P-tile workgroups (vs co-resident M-tile/light workgroups)
# speedup vs baseline: 1.0159x; 1.0017x over previous
_Z6k_prepPKfS0_S0_S0_S0_PfPDF16_S1_S1_S1_S1_S1_Pi:
	s_load_dwordx4 s[20:23], s[0:1], 0x0
	s_cmpk_lt_u32 s2, 0xa1
	s_movk_i32 s3, 0x240
	s_cselect_b32 s26, s3, 0xffffff5f
	s_add_i32 s26, s26, s2
	v_and_b32_e32 v1, 63, v0
	v_lshrrev_b32_e32 v80, 6, v0
	s_cmpk_lt_i32 s26, 0x240
	s_mov_b64 s[4:5], -1
	s_cbranch_scc0 .LBB0_36
	s_cmpk_lt_i32 s26, 0x100
	s_cselect_b64 s[24:25], -1, 0
	s_cbranch_scc0 .Lmy_np
	s_setprio 2
.Lmy_np:
	s_add_i32 s27, s26, 0xffffff00
	s_cmpk_gt_i32 s26, 0xff
	s_cselect_b32 s3, s27, s26
	s_waitcnt lgkmcnt(0)
	s_cselect_b32 s5, s23, s21
	s_cselect_b32 s4, s22, s20
	s_lshl_b32 s6, s3, 2
	s_lshl_b32 s3, s3, 5
	s_and_b32 s28, s3, 0xe0
	s_and_b32 s3, s6, 0xffffffe0
	v_lshrrev_b32_e32 v38, 3, v1
	v_or_b32_e32 v2, s3, v38
	v_ashrrev_i32_e32 v3, 31, v2
	v_lshlrev_b64 v[2:3], 12, v[2:3]
	v_lshl_add_u64 v[2:3], s[4:5], 0, v[2:3]
	v_lshlrev_b32_e32 v34, 9, v80
	v_mov_b32_e32 v35, 0
	v_lshlrev_b32_e32 v4, 4, v0
	v_lshl_add_u64 v[2:3], v[2:3], 0, v[34:35]
	v_and_b32_e32 v36, 0x70, v4
	v_mov_b32_e32 v37, v35
	v_lshl_add_u64 v[70:71], v[2:3], 0, v[36:37]
	v_or_b32_e32 v2, s28, v38
	v_lshlrev_b32_e32 v2, 12, v2
	v_mov_b32_e32 v3, v35
	v_lshl_add_u64 v[2:3], s[22:23], 0, v[2:3]
	s_mov_b32 s4, 0x8000
	v_lshl_add_u64 v[2:3], v[2:3], 0, v[34:35]
	v_add_co_u32_e32 v10, vcc, s4, v70
	v_lshl_add_u64 v[68:69], v[2:3], 0, v[36:37]
	s_nop 0
	v_addc_co_u32_e32 v11, vcc, 0, v71, vcc
	v_add_co_u32_e32 v14, vcc, s4, v68
	s_mov_b32 s4, 0x10000
	s_nop 0
	v_addc_co_u32_e32 v15, vcc, 0, v69, vcc
	v_add_co_u32_e32 v18, vcc, s4, v70
	global_load_dwordx4 v[2:5], v[70:71], off
	global_load_dwordx4 v[6:9], v[68:69], off
	v_addc_co_u32_e32 v19, vcc, 0, v71, vcc
	v_add_co_u32_e32 v22, vcc, s4, v68
	global_load_dwordx4 v[14:17], v[14:15], off
	s_nop 0
	v_addc_co_u32_e32 v23, vcc, 0, v69, vcc
	s_mov_b32 s4, 0x18000
	global_load_dwordx4 v[10:13], v[10:11], off
	v_add_co_u32_e32 v26, vcc, s4, v70
	global_load_dwordx4 v[18:21], v[18:19], off
	s_nop 0
	v_addc_co_u32_e32 v27, vcc, 0, v71, vcc
	global_load_dwordx4 v[22:25], v[22:23], off
	v_add_co_u32_e32 v30, vcc, 0x18000, v68
	global_load_dwordx4 v[26:29], v[26:27], off
	s_nop 0
	v_addc_co_u32_e32 v31, vcc, 0, v69, vcc
	global_load_dwordx4 v[30:33], v[30:31], off
	v_and_b32_e32 v81, 31, v0
	v_mul_u32_u24_e32 v34, 0x2400, v80
	v_lshrrev_b32_e32 v37, 2, v0
	v_mul_u32_u24_e32 v38, 36, v38
	v_or_b32_e32 v34, 32, v34
	v_and_b32_e32 v37, 8, v37
	v_mul_u32_u24_e32 v39, 36, v81
	v_lshlrev_b32_e32 v38, 2, v38
	v_lshlrev_b32_e32 v40, 10, v37
	v_lshlrev_b32_e32 v37, 2, v37
	v_lshlrev_b32_e32 v39, 2, v39
	v_add3_u32 v83, v34, v36, v38
	v_add3_u32 v82, v34, v37, v39
	s_load_dwordx2 s[4:5], s[0:1], 0x18
	v_lshl_or_b32 v34, v80, 17, v40
	s_mov_b32 s7, 0
	s_lshl_b32 s6, s28, 2
	s_and_b64 vcc, exec, s[24:25]
	s_waitcnt lgkmcnt(0)
	v_lshl_add_u64 v[36:37], s[4:5], 0, v[34:35]
	v_lshlrev_b32_e32 v34, 2, v81
	v_lshl_add_u64 v[36:37], v[36:37], 0, s[6:7]
	v_lshl_add_u64 v[66:67], v[36:37], 0, v[34:35]
	s_waitcnt vmcnt(6)
	ds_write_b128 v83, v[6:9] offset:4608
	ds_write_b128 v83, v[2:5]
	s_waitcnt vmcnt(5)
	ds_write_b128 v83, v[14:17] offset:5760
	s_waitcnt vmcnt(4)
	ds_write_b128 v83, v[10:13] offset:1152
	s_waitcnt vmcnt(3)
	ds_write_b128 v83, v[18:21] offset:2304
	s_waitcnt vmcnt(2)
	ds_write_b128 v83, v[22:25] offset:6912
	s_waitcnt vmcnt(1)
	ds_write_b128 v83, v[26:29] offset:3456
	s_waitcnt vmcnt(0)
	ds_write_b128 v83, v[30:33] offset:8064
	ds_read_b96 v[2:4], v82
	ds_read2_b32 v[8:9], v82 offset0:3 offset1:4
	ds_read_b32 v5, v82 offset:28
	ds_read2_b32 v[6:7], v82 offset0:5 offset1:6
	s_waitcnt lgkmcnt(3)
	v_mov_b32_e32 v10, v3
	v_cvt_f16_f32_e32 v3, v2
	v_mov_b32_e32 v11, v4
	s_cbranch_vccz .LBB0_3
	s_movk_i32 s4, 0x1000
	global_load_dword v60, v[66:67], off
	global_load_dword v61, v[66:67], off offset:1024
	global_load_dword v62, v[66:67], off offset:2048
	global_load_dword v63, v[66:67], off offset:3072
	v_add_co_u32_e32 v12, vcc, s4, v66
	v_cvt_f16_f32_e32 v27, v10
	s_nop 0
	v_addc_co_u32_e32 v13, vcc, 0, v67, vcc
	global_load_dword v64, v[12:13], off
	global_load_dword v65, v[12:13], off offset:2048
	global_load_dword v72, v[12:13], off offset:3072
	global_load_dword v73, v[12:13], off offset:1024
	s_waitcnt lgkmcnt(2)
	v_pk_mov_b32 v[16:17], v[10:11], v[8:9] op_sel:[1,0]
	s_waitcnt lgkmcnt(0)
	v_pk_mov_b32 v[18:19], v[8:9], v[6:7] op_sel:[1,0]
	v_cvt_pk_f16_f32 v15, v7, v5
	v_cvt_pk_f16_f32 v13, v16, v17
	v_cvt_pk_f16_f32 v14, v18, v19
	v_cvt_f32_f16_e32 v26, v3
	ds_read_b128 v[32:35], v82 offset:4608
	ds_read_b128 v[36:39], v82 offset:4624
	v_cvt_f32_f16_e32 v20, v15
	v_cvt_f32_f16_sdwa v21, v15 dst_sel:DWORD dst_unused:UNUSED_PAD src0_sel:WORD_1
	v_cvt_f32_f16_e32 v22, v13
	v_cvt_f32_f16_sdwa v23, v13 dst_sel:DWORD dst_unused:UNUSED_PAD src0_sel:WORD_1
	v_cvt_f32_f16_e32 v24, v14
	v_cvt_f32_f16_sdwa v25, v14 dst_sel:DWORD dst_unused:UNUSED_PAD src0_sel:WORD_1
	v_cvt_f32_f16_e32 v47, v27
	s_mov_b32 s4, 0x41800000
	v_mov_b32_e32 v4, v7
	s_movk_i32 s5, 0x4000
	v_cvt_pk_f16_f32 v12, v2, v10
	v_sub_f32_e32 v2, v2, v26
	s_waitcnt lgkmcnt(1)
	v_pk_mul_f32 v[26:27], v[32:33], s[4:5] op_sel_hi:[1,0]
	v_pk_add_f32 v[20:21], v[4:5], v[20:21] neg_lo:[0,1] neg_hi:[0,1]
	v_pk_add_f32 v[16:17], v[16:17], v[22:23] neg_lo:[0,1] neg_hi:[0,1]
	v_pk_add_f32 v[22:23], v[18:19], v[24:25] neg_lo:[0,1] neg_hi:[0,1]
	v_sub_f32_e32 v4, v10, v47
	v_cvt_pk_f16_f32 v40, v26, v27
	v_cvt_pk_f16_f32 v19, v20, v21
	v_cvt_pk_f16_f32 v17, v16, v17
	v_cvt_pk_f16_f32 v18, v22, v23
	v_cvt_pk_f16_f32 v16, v2, v4
	v_cvt_f32_f16_e32 v20, v40
	v_cvt_f32_f16_sdwa v21, v40 dst_sel:DWORD dst_unused:UNUSED_PAD src0_sel:WORD_1
	v_pk_mul_f32 v[28:29], v[34:35], s[4:5] op_sel_hi:[1,0]
	s_waitcnt lgkmcnt(0)
	v_pk_mul_f32 v[30:31], v[36:37], s[4:5] op_sel_hi:[1,0]
	v_pk_mul_f32 v[44:45], v[38:39], s[4:5] op_sel_hi:[1,0]
	v_cvt_pk_f16_f32 v41, v28, v29
	v_cvt_pk_f16_f32 v42, v30, v31
	v_cvt_pk_f16_f32 v43, v44, v45
	v_pk_fma_f32 v[58:59], v[32:33], s[4:5], v[20:21] op_sel_hi:[1,0,1] neg_lo:[0,0,1] neg_hi:[0,0,1]
	v_cvt_f32_f16_e32 v44, v41
	v_mfma_f32_32x32x16_f16 v[18:33], v[16:19], v[40:43], 0
	v_cvt_f32_f16_sdwa v45, v41 dst_sel:DWORD dst_unused:UNUSED_PAD src0_sel:WORD_1
	v_cvt_f32_f16_e32 v46, v42
	v_cvt_f32_f16_sdwa v47, v42 dst_sel:DWORD dst_unused:UNUSED_PAD src0_sel:WORD_1
	v_cvt_f32_f16_e32 v48, v43
	v_cvt_f32_f16_sdwa v49, v43 dst_sel:DWORD dst_unused:UNUSED_PAD src0_sel:WORD_1
	ds_read_b128 v[50:53], v82 offset:64
	ds_read_b128 v[54:57], v82 offset:80
	v_pk_fma_f32 v[16:17], v[34:35], s[4:5], v[44:45] op_sel_hi:[1,0,1] neg_lo:[0,0,1] neg_hi:[0,0,1]
	v_pk_fma_f32 v[36:37], v[36:37], s[4:5], v[46:47] op_sel_hi:[1,0,1] neg_lo:[0,0,1] neg_hi:[0,0,1]
	v_pk_fma_f32 v[38:39], v[38:39], s[4:5], v[48:49] op_sel_hi:[1,0,1] neg_lo:[0,0,1] neg_hi:[0,0,1]
	v_cvt_pk_f16_f32 v35, v16, v17
	v_add_co_u32_e32 v16, vcc, s5, v66
	v_cvt_pk_f16_f32 v34, v58, v59
	v_cvt_pk_f16_f32 v36, v36, v37
	v_cvt_pk_f16_f32 v37, v38, v39
	v_addc_co_u32_e32 v17, vcc, 0, v67, vcc
	s_nop 0
	v_mfma_f32_32x32x16_f16 v[18:33], v[12:15], v[34:37], v[18:33]
	global_load_dword v2, v[16:17], off offset:1024
	global_load_dword v4, v[16:17], off offset:2048
	global_load_dword v78, v[16:17], off offset:3072
	s_waitcnt lgkmcnt(1)
	v_cvt_f16_f32_e32 v16, v50
	v_cvt_f16_f32_e32 v17, v51
	s_waitcnt lgkmcnt(0)
	v_cvt_pk_f16_f32 v74, v54, v55
	v_cvt_f32_f16_e32 v76, v74
	v_cvt_f32_f16_e32 v16, v16
	v_cvt_f32_f16_sdwa v77, v74 dst_sel:DWORD dst_unused:UNUSED_PAD src0_sel:WORD_1
	v_mfma_f32_32x32x16_f16 v[18:33], v[12:15], v[40:43], v[18:33]
	v_cvt_pk_f16_f32 v75, v56, v57
	s_waitcnt vmcnt(9)
	v_cvt_pk_f16_f32 v34, v60, v61
	ds_read_b128 v[58:61], v82 offset:4672
	s_waitcnt vmcnt(7)
	v_cvt_pk_f16_f32 v35, v62, v63
	v_sub_f32_e32 v63, v50, v16
	s_waitcnt vmcnt(4)
	v_cvt_pk_f16_f32 v37, v65, v72
	s_waitcnt vmcnt(3)
	v_cvt_pk_f16_f32 v36, v64, v73
	v_cvt_f32_f16_e32 v64, v17
	v_cvt_pk_f16_f32 v73, v52, v53
	v_mfma_f32_32x32x16_f16 v[34:49], v[12:15], v[34:37], 0
	ds_read_b128 v[12:15], v82 offset:4688
	s_waitcnt lgkmcnt(1)
	v_mul_f32_e64 v16, v58, s4
	v_mul_f32_e64 v17, v59, s4
	v_cvt_pk_f16_f32 v72, v50, v51
	v_cvt_pk_f16_f32 v62, v16, v17
	v_cvt_f32_f16_e32 v16, v62
	v_cvt_f32_f16_sdwa v17, v62 dst_sel:DWORD dst_unused:UNUSED_PAD src0_sel:WORD_1
	v_sub_f32_e32 v50, v51, v64
	v_pk_mul_f32 v[64:65], v[60:61], s[4:5] op_sel_hi:[1,0]
	v_cvt_pk_f16_f32 v50, v63, v50
	v_pk_fma_f32 v[16:17], v[58:59], s[4:5], v[16:17] op_sel_hi:[1,0,1] neg_lo:[0,0,1] neg_hi:[0,0,1]
	v_cvt_pk_f16_f32 v63, v64, v65
	v_cvt_pk_f16_f32 v58, v16, v17
	v_cvt_f32_f16_e32 v16, v73
	v_cvt_f32_f16_sdwa v17, v73 dst_sel:DWORD dst_unused:UNUSED_PAD src0_sel:WORD_1
	v_cvt_f32_f16_e32 v64, v63
	v_cvt_f32_f16_sdwa v65, v63 dst_sel:DWORD dst_unused:UNUSED_PAD src0_sel:WORD_1
	v_pk_add_f32 v[16:17], v[52:53], v[16:17] neg_lo:[0,1] neg_hi:[0,1]
	v_pk_add_f32 v[52:53], v[54:55], v[76:77] neg_lo:[0,1] neg_hi:[0,1]
	v_cvt_f32_f16_e32 v54, v75
	v_cvt_f32_f16_sdwa v55, v75 dst_sel:DWORD dst_unused:UNUSED_PAD src0_sel:WORD_1
	v_cvt_pk_f16_f32 v51, v16, v17
	v_cvt_pk_f16_f32 v52, v52, v53
	v_pk_fma_f32 v[16:17], v[60:61], s[4:5], v[64:65] op_sel_hi:[1,0,1] neg_lo:[0,0,1] neg_hi:[0,0,1]
	v_pk_add_f32 v[54:55], v[56:57], v[54:55] neg_lo:[0,1] neg_hi:[0,1]
	s_waitcnt lgkmcnt(0)
	v_pk_mul_f32 v[60:61], v[12:13], s[4:5] op_sel_hi:[1,0]
	v_cvt_pk_f16_f32 v53, v54, v55
	v_cvt_pk_f16_f32 v64, v60, v61
	v_pk_mul_f32 v[56:57], v[14:15], s[4:5] op_sel_hi:[1,0]
	v_cvt_f32_f16_e32 v54, v64
	v_cvt_f32_f16_sdwa v55, v64 dst_sel:DWORD dst_unused:UNUSED_PAD src0_sel:WORD_1
	v_cvt_pk_f16_f32 v65, v56, v57
	v_cvt_pk_f16_f32 v59, v16, v17
	v_pk_fma_f32 v[12:13], v[12:13], s[4:5], v[54:55] op_sel_hi:[1,0,1] neg_lo:[0,0,1] neg_hi:[0,0,1]
	v_mfma_f32_32x32x16_f16 v[18:33], v[50:53], v[62:65], v[18:33]
	v_cvt_f32_f16_e32 v50, v65
	v_cvt_f32_f16_sdwa v51, v65 dst_sel:DWORD dst_unused:UNUSED_PAD src0_sel:WORD_1
	v_cvt_pk_f16_f32 v60, v12, v13
	v_fma_f32 v12, v14, s4, -v50
	v_fma_f32 v13, v15, s4, -v51
	s_movk_i32 s4, 0x5000
	v_cvt_pk_f16_f32 v61, v12, v13
	v_add_co_u32_e32 v12, vcc, s4, v66
	s_nop 0
	v_mfma_f32_32x32x16_f16 v[18:33], v[72:75], v[58:61], v[18:33]
	v_addc_co_u32_e32 v13, vcc, 0, v67, vcc
	global_load_dword v14, v[12:13], off
	global_load_dword v15, v[12:13], off offset:2048
	global_load_dword v16, v[12:13], off offset:3072
	global_load_dword v17, v[12:13], off offset:1024
	s_mov_b64 s[4:5], 0
	global_load_dword v12, v[12:13], off offset:-4096
	s_waitcnt vmcnt(5)
	v_cvt_pk_f16_f32 v13, v4, v78
	v_mfma_f32_32x32x16_f16 v[18:33], v[72:75], v[62:65], v[18:33]
	s_waitcnt vmcnt(2)
	v_cvt_pk_f16_f32 v15, v15, v16
	s_waitcnt vmcnt(1)
	v_cvt_pk_f16_f32 v14, v14, v17
	s_waitcnt vmcnt(0)
	v_cvt_pk_f16_f32 v12, v12, v2
	s_nop 1
	v_mfma_f32_32x32x16_f16 v[34:49], v[72:75], v[12:15], v[34:49]
	s_branch .LBB0_4
